# global wave index interleaved across CUs (wave*G+vcu) so grid-stride phase tails are spread over all CUs
# speedup vs baseline: 1.0040x; 1.0040x over previous
.LBB0_13:
	v_writelane_b32 v251, s12, 16
	v_writelane_b32 v251, s10, 18
	s_nop 1
	v_writelane_b32 v251, s11, 19
	s_or_b64 exec, exec, s[2:3]
	s_load_dwordx16 s[36:51], s[0:1], 0x0
	s_load_dword s3, s[0:1], 0xe0
	v_readlane_b32 s5, v251, 4
	s_lshr_b32 s8, s6, 6
	s_nop 0
	s_nop 0
	v_writelane_b32 v251, s8, 20
	s_nop 0
	s_waitcnt lgkmcnt(0)
	s_mul_i32 s2, s8, s3
	s_add_i32 s4, s2, s5
	s_mov_b32 s2, s4
	s_lshl_b32 s17, s3, 3
	v_writelane_b32 v251, s2, 21
	s_mov_b32 s16, s4
	v_mov_b32_e32 v50, v246
	v_writelane_b32 v251, s3, 22
	v_writelane_b32 v251, s17, 23
	s_movk_i32 s2, 0x1400
	s_mov_b32 s28, s5
	v_writelane_b32 v251, s3, 24
	v_cmp_gt_i32_e32 vcc, s2, v50
	s_and_saveexec_b64 s[2:3], vcc
	s_cbranch_execz .LBB0_16
	v_mov_b32_e32 v2, s38
	v_mov_b32_e32 v3, s39
	v_ashrrev_i32_e32 v51, 31, v50
	v_lshl_add_u32 v1, v50, 2, 0
	v_lshl_add_u64 v[2:3], v[50:51], 2, v[2:3]
	s_mov_b64 s[4:5], 0
	s_movk_i32 s9, 0x1000
	v_mov_b32_e32 v5, 0
	s_mov_b64 s[6:7], 0x800
	s_movk_i32 s10, 0x11ff
	v_mov_b32_e32 v6, v50

.LBB0_271:
	s_or_b64 exec, exec, s[2:3]
	v_cvt_f32_u32_e32 v0, v3
	s_waitcnt vmcnt(0)
	v_readfirstlane_b32 s2, v4
	v_sub_u32_e32 v4, 0, v3
	v_rcp_iflag_f32_e32 v0, v0
	v_add_u32_e32 v5, s2, v1
	v_mul_f32_e32 v0, 0x4f7ffffe, v0
	v_cvt_u32_f32_e32 v0, v0
	v_mul_lo_u32 v1, v4, v0
	v_mul_hi_u32 v1, v0, v1
	v_add_u32_e32 v0, v0, v1
	v_mul_hi_u32 v0, v5, v0
	v_mul_lo_u32 v1, v0, v3
	v_sub_u32_e32 v1, v5, v1
	v_add_u32_e32 v4, 1, v0
	v_cmp_ge_u32_e32 vcc, v1, v3
	s_nop 1
	v_cndmask_b32_e32 v0, v0, v4, vcc
	v_sub_u32_e32 v4, v1, v3
	v_cndmask_b32_e32 v1, v1, v4, vcc
	v_add_u32_e32 v4, 1, v0
	v_cmp_ge_u32_e32 vcc, v1, v3
	s_nop 1
	v_cndmask_b32_e32 v1, v0, v4, vcc
	v_mul_lo_u32 v4, v3, v1
	v_add_u32_e32 v0, 1, v5
	v_add_u32_e32 v3, v4, v3
	v_cmp_ne_u32_e32 vcc, v0, v3
	s_and_saveexec_b64 s[2:3], vcc
	s_xor_b64 s[2:3], exec, s[2:3]
	s_cbranch_execz .LBB0_285
	v_readlane_b32 s4, v251, 16
	s_waitcnt lgkmcnt(0)
	v_mov_b32_e32 v2, 0
	v_readlane_b32 s5, v251, 17
	s_nop 4
	global_load_dword v0, v2, s[4:5] sc1
	s_waitcnt vmcnt(0)
	v_cmp_eq_u32_e32 vcc, v0, v1
	s_and_saveexec_b64 s[4:5], vcc
	s_cbranch_execz .LBB0_284
	s_mov_b32 s16, 1
	s_mov_b64 s[6:7], 0
	s_branch .LBB0_275

.LBB0_277:
	v_readlane_b32 s10, v251, 16
	v_readlane_b32 s11, v251, 17
	s_add_i32 s16, s16, 1
	s_mov_b64 s[12:13], -1
	s_nop 2
	global_load_dword v0, v2, s[10:11] sc1
	s_waitcnt vmcnt(0)
	v_cmp_ne_u32_e32 vcc, v0, v1
	s_orn2_b64 s[10:11], vcc, exec
	s_branch .LBB0_274

.LBB0_419:
	s_or_b64 exec, exec, s[2:3]
	v_cvt_f32_u32_e32 v5, v3
	s_waitcnt vmcnt(0)
	v_readfirstlane_b32 s2, v4
	v_sub_u32_e32 v4, 0, v3
	v_rcp_iflag_f32_e32 v5, v5
	v_add_u32_e32 v6, s2, v1
	v_mul_f32_e32 v5, 0x4f7ffffe, v5
	v_cvt_u32_f32_e32 v5, v5
	v_mul_lo_u32 v1, v4, v5
	v_mul_hi_u32 v1, v5, v1
	v_add_u32_e32 v1, v5, v1
	v_mul_hi_u32 v1, v6, v1
	v_mul_lo_u32 v4, v1, v3
	v_sub_u32_e32 v4, v6, v4
	v_add_u32_e32 v5, 1, v1
	v_cmp_ge_u32_e32 vcc, v4, v3
	s_nop 1
	v_cndmask_b32_e32 v1, v1, v5, vcc
	v_sub_u32_e32 v5, v4, v3
	v_cndmask_b32_e32 v4, v4, v5, vcc
	v_add_u32_e32 v5, 1, v1
	v_cmp_ge_u32_e32 vcc, v4, v3
	v_add_u32_e32 v4, 1, v6
	s_nop 0
	v_cndmask_b32_e32 v1, v1, v5, vcc
	v_mul_lo_u32 v5, v3, v1
	v_add_u32_e32 v3, v5, v3
	v_cmp_ne_u32_e32 vcc, v4, v3
	s_and_saveexec_b64 s[2:3], vcc
	s_xor_b64 s[2:3], exec, s[2:3]
	s_cbranch_execz .LBB0_433
	v_readlane_b32 s4, v251, 16
	v_readlane_b32 s5, v251, 17
	s_waitcnt lgkmcnt(0)
	s_nop 3
	global_load_dword v2, v67, s[4:5] sc1
	s_waitcnt vmcnt(0)
	v_cmp_eq_u32_e32 vcc, v2, v1
	s_and_saveexec_b64 s[4:5], vcc
	s_cbranch_execz .LBB0_432
	s_mov_b32 s8, 1
	s_mov_b64 s[36:37], 0
	s_branch .LBB0_423

.LBB0_425:
	v_readlane_b32 s10, v251, 16
	v_readlane_b32 s11, v251, 17
	s_add_i32 s8, s8, 1
	s_mov_b64 s[42:43], -1
	s_nop 2
	global_load_dword v2, v67, s[10:11] sc1
	s_waitcnt vmcnt(0)
	v_cmp_ne_u32_e32 vcc, v2, v1
	s_orn2_b64 s[40:41], vcc, exec
	s_branch .LBB0_422

.LBB0_1717:
	s_or_b64 exec, exec, s[2:3]
	v_cvt_f32_u32_e32 v5, v3
	s_waitcnt vmcnt(0)
	v_readfirstlane_b32 s2, v4
	v_sub_u32_e32 v4, 0, v3
	v_rcp_iflag_f32_e32 v5, v5
	v_add_u32_e32 v6, s2, v1
	v_mul_f32_e32 v5, 0x4f7ffffe, v5
	v_cvt_u32_f32_e32 v5, v5
	v_mul_lo_u32 v1, v4, v5
	v_mul_hi_u32 v1, v5, v1
	v_add_u32_e32 v1, v5, v1
	v_mul_hi_u32 v1, v6, v1
	v_mul_lo_u32 v4, v1, v3
	v_sub_u32_e32 v4, v6, v4
	v_add_u32_e32 v5, 1, v1
	v_cmp_ge_u32_e32 vcc, v4, v3
	s_nop 1
	v_cndmask_b32_e32 v1, v1, v5, vcc
	v_sub_u32_e32 v5, v4, v3
	v_cndmask_b32_e32 v4, v4, v5, vcc
	v_add_u32_e32 v5, 1, v1
	v_cmp_ge_u32_e32 vcc, v4, v3
	v_add_u32_e32 v4, 1, v6
	s_nop 0
	v_cndmask_b32_e32 v1, v1, v5, vcc
	v_mul_lo_u32 v5, v3, v1
	v_add_u32_e32 v3, v5, v3
	v_cmp_ne_u32_e32 vcc, v4, v3
	s_and_saveexec_b64 s[2:3], vcc
	s_xor_b64 s[2:3], exec, s[2:3]
	s_cbranch_execz .LBB0_1731
	v_readlane_b32 s4, v251, 16
	v_readlane_b32 s5, v251, 17
	s_waitcnt lgkmcnt(0)
	s_nop 3
	global_load_dword v2, v67, s[4:5] sc1
	s_waitcnt vmcnt(0)
	v_cmp_eq_u32_e32 vcc, v2, v1
	s_and_saveexec_b64 s[4:5], vcc
	s_cbranch_execz .LBB0_1730
	s_mov_b32 s10, 1
	s_mov_b64 s[36:37], 0
	s_branch .LBB0_1721

.LBB0_1723:
	v_readlane_b32 s14, v251, 16
	v_readlane_b32 s15, v251, 17
	s_add_i32 s10, s10, 1
	s_mov_b64 s[42:43], -1
	s_nop 2
	global_load_dword v2, v67, s[14:15] sc1
	s_waitcnt vmcnt(0)
	v_cmp_ne_u32_e32 vcc, v2, v1
	s_orn2_b64 s[40:41], vcc, exec
	s_branch .LBB0_1720
